# speedup vs baseline: 1.1049x; 1.0020x over previous
.LBB0_6:
	s_or_b64 exec, exec, s[6:7]
	s_load_dwordx2 s[0:1], s[0:1], 0x18
	s_waitcnt vmcnt(0)
	v_mul_f32_e32 v19, v14, v14
	v_mul_f32_e32 v21, v15, v15
	v_mul_f32_e32 v23, v16, v16
	v_mul_f32_e32 v25, v17, v17
	v_mov_b32_e32 v18, v14
	v_mov_b32_e32 v20, v15
	v_mov_b32_e32 v22, v16
	v_mov_b32_e32 v24, v17
	v_pk_add_f32 v[14:15], v[18:19], v[20:21]
	v_pk_add_f32 v[16:17], v[22:23], v[24:25]
	s_nop 0
	v_pk_add_f32 v[14:15], v[14:15], v[16:17]
	v_mul_f32_e32 v19, v10, v10
	v_mul_f32_e32 v21, v11, v11
	v_mul_f32_e32 v23, v12, v12
	v_mul_f32_e32 v25, v13, v13
	v_mov_b32_e32 v18, v10
	v_mov_b32_e32 v20, v11
	v_mov_b32_e32 v22, v12
	v_mov_b32_e32 v24, v13
	v_pk_add_f32 v[10:11], v[18:19], v[20:21]
	v_pk_add_f32 v[12:13], v[22:23], v[24:25]
	s_nop 0
	v_pk_add_f32 v[10:11], v[10:11], v[12:13]
	v_mul_f32_e32 v19, v6, v6
	v_mul_f32_e32 v21, v7, v7
	v_mul_f32_e32 v23, v8, v8
	v_mul_f32_e32 v25, v9, v9
	v_mov_b32_e32 v18, v6
	v_mov_b32_e32 v20, v7
	v_mov_b32_e32 v22, v8
	v_mov_b32_e32 v24, v9
	v_pk_add_f32 v[6:7], v[18:19], v[20:21]
	v_pk_add_f32 v[8:9], v[22:23], v[24:25]
	s_nop 0
	v_pk_add_f32 v[6:7], v[6:7], v[8:9]
	v_mul_f32_e32 v19, v2, v2
	v_mul_f32_e32 v21, v3, v3
	v_mul_f32_e32 v23, v4, v4
	v_mul_f32_e32 v25, v5, v5
	v_mov_b32_e32 v18, v2
	v_mov_b32_e32 v20, v3
	v_mov_b32_e32 v22, v4
	v_mov_b32_e32 v24, v5
	v_pk_add_f32 v[2:3], v[18:19], v[20:21]
	v_pk_add_f32 v[4:5], v[22:23], v[24:25]
	s_nop 0
	v_pk_add_f32 v[2:3], v[2:3], v[4:5]
	v_mov_b32_e32 v18, v14
	v_mov_b32_e32 v19, v15
	v_mov_b32_e32 v20, v10
	v_mov_b32_e32 v21, v11
	v_mov_b32_e32 v22, v6
	v_mov_b32_e32 v23, v7
	v_mov_b32_e32 v24, v2
	v_mov_b32_e32 v25, v3
	v_permlane32_swap_b32_e32 v18, v14
	v_permlane32_swap_b32_e32 v19, v15
	v_permlane32_swap_b32_e32 v20, v10
	v_permlane32_swap_b32_e32 v21, v11
	v_permlane32_swap_b32_e32 v22, v6
	v_permlane32_swap_b32_e32 v23, v7
	v_permlane32_swap_b32_e32 v24, v2
	v_permlane32_swap_b32_e32 v25, v3
	v_add_f32_e32 v14, v14, v18
	v_add_f32_e32 v15, v15, v19
	v_add_f32_e32 v10, v10, v20
	v_add_f32_e32 v11, v11, v21
	v_add_f32_e32 v6, v6, v22
	v_add_f32_e32 v7, v7, v23
	v_add_f32_e32 v2, v2, v24
	v_add_f32_e32 v3, v3, v25
	v_mov_b32_e32 v18, v14
	v_mov_b32_e32 v19, v15
	v_mov_b32_e32 v20, v10
	v_mov_b32_e32 v21, v11
	v_mov_b32_e32 v22, v6
	v_mov_b32_e32 v23, v7
	v_mov_b32_e32 v24, v2
	v_mov_b32_e32 v25, v3
	v_permlane16_swap_b32_e32 v18, v14
	v_permlane16_swap_b32_e32 v19, v15
	v_permlane16_swap_b32_e32 v20, v10
	v_permlane16_swap_b32_e32 v21, v11
	v_permlane16_swap_b32_e32 v22, v6
	v_permlane16_swap_b32_e32 v23, v7
	v_permlane16_swap_b32_e32 v24, v2
	v_permlane16_swap_b32_e32 v25, v3
	v_add_f32_e32 v14, v14, v18
	v_add_f32_e32 v15, v15, v19
	v_add_f32_e32 v10, v10, v20
	v_add_f32_e32 v11, v11, v21
	v_add_f32_e32 v6, v6, v22
	v_add_f32_e32 v7, v7, v23
	v_add_f32_e32 v2, v2, v24
	v_add_f32_e32 v3, v3, v25
	v_add_f32_dpp v14, v14, v14 row_shl:8 row_mask:0xf bank_mask:0xf
	v_add_f32_dpp v15, v15, v15 row_shl:8 row_mask:0xf bank_mask:0xf
	v_add_f32_dpp v10, v10, v10 row_shl:8 row_mask:0xf bank_mask:0xf
	v_add_f32_dpp v11, v11, v11 row_shl:8 row_mask:0xf bank_mask:0xf
	v_add_f32_dpp v6, v6, v6 row_shl:8 row_mask:0xf bank_mask:0xf
	v_add_f32_dpp v7, v7, v7 row_shl:8 row_mask:0xf bank_mask:0xf
	v_add_f32_dpp v2, v2, v2 row_shl:8 row_mask:0xf bank_mask:0xf
	v_add_f32_dpp v3, v3, v3 row_shl:8 row_mask:0xf bank_mask:0xf
	v_add_f32_dpp v14, v14, v14 row_shl:4 row_mask:0xf bank_mask:0xf
	v_add_f32_dpp v15, v15, v15 row_shl:4 row_mask:0xf bank_mask:0xf
	v_add_f32_dpp v10, v10, v10 row_shl:4 row_mask:0xf bank_mask:0xf
	v_add_f32_dpp v11, v11, v11 row_shl:4 row_mask:0xf bank_mask:0xf
	v_add_f32_dpp v6, v6, v6 row_shl:4 row_mask:0xf bank_mask:0xf
	v_add_f32_dpp v7, v7, v7 row_shl:4 row_mask:0xf bank_mask:0xf
	v_add_f32_dpp v2, v2, v2 row_shl:4 row_mask:0xf bank_mask:0xf
	v_add_f32_dpp v3, v3, v3 row_shl:4 row_mask:0xf bank_mask:0xf
	v_add_f32_dpp v14, v14, v14 row_shl:2 row_mask:0xf bank_mask:0xf
	v_add_f32_dpp v15, v15, v15 row_shl:2 row_mask:0xf bank_mask:0xf
	v_add_f32_dpp v10, v10, v10 row_shl:2 row_mask:0xf bank_mask:0xf
	v_add_f32_dpp v11, v11, v11 row_shl:2 row_mask:0xf bank_mask:0xf
	v_add_f32_dpp v6, v6, v6 row_shl:2 row_mask:0xf bank_mask:0xf
	v_add_f32_dpp v7, v7, v7 row_shl:2 row_mask:0xf bank_mask:0xf
	v_add_f32_dpp v2, v2, v2 row_shl:2 row_mask:0xf bank_mask:0xf
	v_add_f32_dpp v3, v3, v3 row_shl:2 row_mask:0xf bank_mask:0xf
	v_add_f32_dpp v14, v14, v14 row_shl:1 row_mask:0xf bank_mask:0xf
	v_add_f32_dpp v15, v15, v15 row_shl:1 row_mask:0xf bank_mask:0xf
	v_add_f32_dpp v10, v10, v10 row_shl:1 row_mask:0xf bank_mask:0xf
	v_add_f32_dpp v11, v11, v11 row_shl:1 row_mask:0xf bank_mask:0xf
	v_add_f32_dpp v6, v6, v6 row_shl:1 row_mask:0xf bank_mask:0xf
	v_add_f32_dpp v7, v7, v7 row_shl:1 row_mask:0xf bank_mask:0xf
	v_add_f32_dpp v2, v2, v2 row_shl:1 row_mask:0xf bank_mask:0xf
	v_add_f32_dpp v3, v3, v3 row_shl:1 row_mask:0xf bank_mask:0xf
	v_and_b32_e32 v26, 63, v0
	v_lshrrev_b32_e32 v22, 3, v0
	v_cmp_eq_u32_e32 vcc, 0, v26
	s_and_saveexec_b64 s[2:3], vcc
	ds_write_b64 v22, v[14:15]
	ds_write_b64 v22, v[10:11] offset:128
	ds_write_b64 v22, v[6:7] offset:256
	ds_write_b64 v22, v[2:3] offset:384
	s_or_b64 exec, exec, s[2:3]
	v_cmp_gt_u32_e32 vcc, 8, v0
	s_waitcnt lgkmcnt(0)
	s_barrier
	s_and_saveexec_b64 s[2:3], vcc
	s_cbranch_execz .LBB0_16
	v_lshlrev_b32_e32 v1, 6, v0
	ds_read_b128 v[2:5], v1
	ds_read_b128 v[6:9], v1 offset:16
	ds_read_b128 v[10:13], v1 offset:32
	ds_read_b128 v[14:17], v1 offset:48
	v_lshl_or_b32 v0, s4, 3, v0
	s_waitcnt lgkmcnt(3)
	v_cvt_f64_f32_e32 v[18:19], v2
	v_cvt_f64_f32_e32 v[2:3], v3
	v_add_f64 v[18:19], v[18:19], 0
	v_add_f64 v[2:3], v[2:3], 0
	v_cvt_f64_f32_e32 v[20:21], v4
	v_cvt_f64_f32_e32 v[4:5], v5
	v_add_f64 v[18:19], v[18:19], v[20:21]
	v_add_f64 v[2:3], v[2:3], v[4:5]
	s_waitcnt lgkmcnt(2)
	v_cvt_f64_f32_e32 v[4:5], v6
	v_cvt_f64_f32_e32 v[6:7], v7
	v_add_f64 v[4:5], v[18:19], v[4:5]
	v_add_f64 v[2:3], v[2:3], v[6:7]
	v_cvt_f64_f32_e32 v[6:7], v8
	v_add_f64 v[4:5], v[4:5], v[6:7]
	v_cvt_f64_f32_e32 v[6:7], v9
	v_add_f64 v[2:3], v[2:3], v[6:7]
	s_waitcnt lgkmcnt(1)
	v_cvt_f64_f32_e32 v[6:7], v10
	v_add_f64 v[4:5], v[4:5], v[6:7]
	v_cvt_f64_f32_e32 v[6:7], v11
	v_add_f64 v[2:3], v[2:3], v[6:7]
	v_cvt_f64_f32_e32 v[6:7], v12
	v_add_f64 v[4:5], v[4:5], v[6:7]
	v_cvt_f64_f32_e32 v[6:7], v13
	v_add_f64 v[2:3], v[2:3], v[6:7]
	s_waitcnt lgkmcnt(0)
	v_cvt_f64_f32_e32 v[6:7], v14
	v_add_f64 v[4:5], v[4:5], v[6:7]
	v_cvt_f64_f32_e32 v[6:7], v15
	v_ashrrev_i32_e32 v1, 31, v0
	v_add_f64 v[6:7], v[2:3], v[6:7]
	v_cvt_f64_f32_e32 v[2:3], v16
	v_lshlrev_b64 v[0:1], 10, v[0:1]
	v_add_f64 v[2:3], v[4:5], v[2:3]
	v_cvt_f64_f32_e32 v[4:5], v17
	v_lshl_add_u64 v[0:1], s[0:1], 0, v[0:1]
	s_lshl_b32 s0, s12, 4
	s_mov_b32 s1, 0
	v_add_f64 v[4:5], v[6:7], v[4:5]
	v_lshl_add_u64 v[0:1], v[0:1], 0, s[0:1]
	global_store_dwordx4 v[0:1], v[2:5], off

.LBB1_10:
	s_or_b64 exec, exec, s[14:15]
	global_load_dwordx4 v[34:37], v[138:139], off offset:1024
	global_load_dwordx4 v[38:41], v[138:139], off offset:1056
	global_load_dwordx4 v[42:45], v[138:139], off offset:1088
	global_load_dwordx4 v[46:49], v[138:139], off offset:1120
	ds_read_b64_tr_b16 v[148:149], v140
	ds_read_b64_tr_b16 v[150:151], v140 offset:1024
	ds_read_b64_tr_b16 v[154:155], v140 offset:1536
	ds_read_b64_tr_b16 v[152:153], v140 offset:512
	v_cmp_eq_u32_e32 vcc, 0, v146
	v_rcp_f32_e32 v138, v147
	s_mov_b32 s4, 0x40000
	s_mov_b32 s20, 0x41000
	s_lshl_b64 s[14:15], s[6:7], 20
	s_lshl_b32 s19, s3, 8
	s_add_u32 s14, s10, s14
	s_mov_b32 s17, 0xc0c0400
	s_mov_b32 s18, 0x4000c0c
	s_waitcnt vmcnt(0) lgkmcnt(2)
	v_mfma_f32_32x32x16_bf16 v[50:65], v[126:129], v[148:151], v[34:49]
	s_waitcnt lgkmcnt(0)
	v_mfma_f32_32x32x16_bf16 v[34:49], v[126:129], v[152:155], v[34:49]
	ds_read_b64_tr_b16 v[126:127], v140 offset:2048
	ds_read_b64_tr_b16 v[128:129], v140 offset:3072
	ds_read_b64_tr_b16 v[150:151], v140 offset:3584
	ds_read_b64_tr_b16 v[148:149], v140 offset:2560
	s_waitcnt lgkmcnt(2)
	v_mfma_f32_32x32x16_bf16 v[50:65], v[122:125], v[126:129], v[50:65]
	s_waitcnt lgkmcnt(0)
	v_mfma_f32_32x32x16_bf16 v[34:49], v[122:125], v[148:151], v[34:49]
	ds_read_b64_tr_b16 v[122:123], v140 offset:4096
	ds_read_b64_tr_b16 v[124:125], v140 offset:5120
	ds_read_b64_tr_b16 v[128:129], v140 offset:5632
	ds_read_b64_tr_b16 v[126:127], v140 offset:4608
	s_waitcnt lgkmcnt(2)
	v_mfma_f32_32x32x16_bf16 v[50:65], v[114:117], v[122:125], v[50:65]
	s_waitcnt lgkmcnt(0)
	v_mfma_f32_32x32x16_bf16 v[34:49], v[114:117], v[126:129], v[34:49]
	ds_read_b64_tr_b16 v[114:115], v140 offset:6144
	ds_read_b64_tr_b16 v[116:117], v140 offset:7168
	ds_read_b64_tr_b16 v[124:125], v140 offset:7680
	ds_read_b64_tr_b16 v[122:123], v140 offset:6656
	v_rcp_f32_e32 v128, v135
	v_lshlrev_b32_e32 v126, 11, v1
	v_mov_b32_e32 v127, 0
	v_mov_b32_e32 v135, v127
	v_mov_b32_e32 v129, 0x4b400000
	s_waitcnt lgkmcnt(2)
	v_mfma_f32_32x32x16_bf16 v[50:65], v[118:121], v[114:117], v[50:65]
	s_waitcnt lgkmcnt(0)
	v_mfma_f32_32x32x16_bf16 v[34:49], v[118:121], v[122:125], v[34:49]
	ds_read_b64_tr_b16 v[114:115], v140 offset:8192
	ds_read_b64_tr_b16 v[116:117], v140 offset:9216
	ds_read_b64_tr_b16 v[120:121], v140 offset:9728
	ds_read_b64_tr_b16 v[118:119], v140 offset:8704
	s_waitcnt lgkmcnt(2)
	v_mfma_f32_32x32x16_bf16 v[50:65], v[110:113], v[114:117], v[50:65]
	s_waitcnt lgkmcnt(0)
	v_mfma_f32_32x32x16_bf16 v[34:49], v[110:113], v[118:121], v[34:49]
	ds_read_b64_tr_b16 v[110:111], v140 offset:10240
	ds_read_b64_tr_b16 v[112:113], v140 offset:11264
	ds_read_b64_tr_b16 v[116:117], v140 offset:11776
	ds_read_b64_tr_b16 v[114:115], v140 offset:10752
	s_waitcnt lgkmcnt(2)
	v_mfma_f32_32x32x16_bf16 v[50:65], v[106:109], v[110:113], v[50:65]
	s_waitcnt lgkmcnt(0)
	v_mfma_f32_32x32x16_bf16 v[34:49], v[106:109], v[114:117], v[34:49]
	ds_read_b64_tr_b16 v[106:107], v140 offset:12288
	ds_read_b64_tr_b16 v[108:109], v140 offset:13312
	ds_read_b64_tr_b16 v[112:113], v140 offset:13824
	ds_read_b64_tr_b16 v[110:111], v140 offset:12800
	s_waitcnt lgkmcnt(2)
	v_mfma_f32_32x32x16_bf16 v[50:65], v[102:105], v[106:109], v[50:65]
	ds_read_b64_tr_b16 v[106:107], v140 offset:14336
	ds_read_b64_tr_b16 v[108:109], v140 offset:15360
	ds_read_b64_tr_b16 v[116:117], v140 offset:15872
	ds_read_b64_tr_b16 v[114:115], v140 offset:14848
	ds_read_b64_tr_b16 v[118:119], v140 offset:16384
	ds_read_b64_tr_b16 v[120:121], v140 offset:17408
	ds_read_b64_tr_b16 v[124:125], v140 offset:17920
	ds_read_b64_tr_b16 v[122:123], v140 offset:16896
	s_waitcnt lgkmcnt(8)
	v_mfma_f32_32x32x16_bf16 v[34:49], v[102:105], v[110:113], v[34:49]
	s_waitcnt lgkmcnt(6)
	v_mfma_f32_32x32x16_bf16 v[50:65], v[98:101], v[106:109], v[50:65]
	ds_read_b64_tr_b16 v[102:103], v140 offset:18432
	ds_read_b64_tr_b16 v[104:105], v140 offset:19456
	ds_read_b64_tr_b16 v[108:109], v140 offset:19968
	ds_read_b64_tr_b16 v[106:107], v140 offset:18944
	s_waitcnt lgkmcnt(8)
	v_mfma_f32_32x32x16_bf16 v[34:49], v[98:101], v[114:117], v[34:49]
	ds_read_b64_tr_b16 v[98:99], v140 offset:20480
	ds_read_b64_tr_b16 v[100:101], v140 offset:21504
	ds_read_b64_tr_b16 v[112:113], v140 offset:22016
	ds_read_b64_tr_b16 v[110:111], v140 offset:20992
	ds_read_b64_tr_b16 v[146:147], v140 offset:22528
	ds_read_b64_tr_b16 v[148:149], v140 offset:23552
	ds_read_b64_tr_b16 v[152:153], v140 offset:24064
	ds_read_b64_tr_b16 v[150:151], v140 offset:23040
	s_waitcnt lgkmcnt(14)
	v_mfma_f32_32x32x16_bf16 v[50:65], v[94:97], v[118:121], v[50:65]
	ds_read_b64_tr_b16 v[118:119], v140 offset:24576
	ds_read_b64_tr_b16 v[120:121], v140 offset:25600
	ds_read_b64_tr_b16 v[156:157], v140 offset:26112
	ds_read_b64_tr_b16 v[154:155], v140 offset:25088
	ds_read_b64_tr_b16 v[158:159], v140 offset:26624
	ds_read_b64_tr_b16 v[160:161], v140 offset:27648
	ds_read_b64_tr_b16 v[164:165], v140 offset:28160
	ds_read_b64_tr_b16 v[162:163], v140 offset:27136
	ds_read_b64_tr_b16 v[166:167], v140 offset:28672
	ds_read_b64_tr_b16 v[168:169], v140 offset:29696
	ds_read_b64_tr_b16 v[172:173], v140 offset:30208
	ds_read_b64_tr_b16 v[170:171], v140 offset:29184
	ds_read_b64_tr_b16 v[174:175], v140 offset:30720
	ds_read_b64_tr_b16 v[176:177], v140 offset:31744
	ds_read_b64_tr_b16 v[180:181], v140 offset:32256
	ds_read_b64_tr_b16 v[178:179], v140 offset:31232
	s_waitcnt lgkmcnt(14)
	v_mfma_f32_32x32x16_bf16 v[34:49], v[94:97], v[122:125], v[34:49]
	v_mul_f32_e32 v94, 0x42fe0000, v128
	v_mul_f32_e32 v94, 0x3f7fffff, v94
	v_fmaak_f32 v97, v23, v94, 0x4b400000
	v_fmaak_f32 v95, v19, v94, 0x4b400000
	v_fmaak_f32 v96, v18, v94, 0x4b400000
	v_fmaak_f32 v21, v21, v94, 0x4b400000
	v_fmaak_f32 v20, v20, v94, 0x4b400000
	v_mfma_f32_32x32x16_bf16 v[50:65], v[90:93], v[102:105], v[50:65]
	v_fmaak_f32 v102, v22, v94, 0x4b400000
	v_add_co_u32_e64 v22, s[4:5], s4, v132
	v_fmaak_f32 v104, v24, v94, 0x4b400000
	s_nop 0
	v_addc_co_u32_e64 v23, s[4:5], 0, v133, s[4:5]
	v_add_co_u32_e64 v24, s[4:5], s20, v132
	v_mfma_f32_32x32x16_bf16 v[34:49], v[90:93], v[106:109], v[34:49]
	v_fmaak_f32 v103, v25, v94, 0x4b400000
	v_addc_co_u32_e64 v25, s[4:5], 0, v133, s[4:5]
	s_addc_u32 s5, s11, s15
	s_add_u32 s4, s14, s19
	s_addc_u32 s5, s5, 0
	v_lshl_add_u64 v[18:19], s[4:5], 0, v[126:127]
	v_mfma_f32_32x32x16_bf16 v[50:65], v[86:89], v[98:101], v[50:65]
	v_fmaak_f32 v27, v27, v94, 0x4b400000
	v_fmaak_f32 v26, v26, v94, 0x4b400000
	v_fmaak_f32 v29, v29, v94, 0x4b400000
	v_fmaak_f32 v28, v28, v94, 0x4b400000
	v_fmaak_f32 v31, v31, v94, 0x4b400000
	v_fmaak_f32 v30, v30, v94, 0x4b400000
	v_fmaak_f32 v98, v33, v94, 0x4b400000
	v_mfma_f32_32x32x16_bf16 v[34:49], v[86:89], v[110:113], v[34:49]
	v_fmaak_f32 v94, v32, v94, 0x4b400000
	v_lshl_add_u64 v[32:33], v[18:19], 0, v[134:135]
	v_perm_b32 v18, v95, v96, s17
	v_perm_b32 v19, v21, v20, s18
	v_perm_b32 v20, v97, v102, s17
	v_perm_b32 v21, v103, v104, s18
	v_or_b32_e32 v18, v18, v19
	v_mfma_f32_32x32x16_bf16 v[50:65], v[82:85], v[146:149], v[50:65]
	v_or_b32_e32 v19, v20, v21
	v_mul_f32_e32 v20, 0x42fe0000, v138
	v_mul_f32_e32 v126, 0x3f7fffff, v20
	s_mov_b32 s4, 0x42000
	v_perm_b32 v21, v31, v30, s17
	v_fmaak_f32 v128, v3, v126, 0x4b400000
	v_perm_b32 v3, v98, v94, s18
	v_mfma_f32_32x32x16_bf16 v[34:49], v[82:85], v[150:153], v[34:49]
	v_fmaak_f32 v134, v2, v126, 0x4b400000
	v_add_co_u32_e64 v2, s[4:5], s4, v132
	v_perm_b32 v26, v27, v26, s17
	v_perm_b32 v27, v29, v28, s18
	v_or_b32_e32 v21, v21, v3
	v_addc_co_u32_e64 v3, s[4:5], 0, v133, s[4:5]
	v_mfma_f32_32x32x16_bf16 v[50:65], v[70:73], v[118:121], v[50:65]
	v_or_b32_e32 v20, v26, v27
	s_mov_b32 s4, 0x43000
	global_load_dwordx4 v[114:117], v[22:23], off offset:1024
	global_load_dwordx4 v[110:113], v[22:23], off offset:2048
	global_load_dwordx4 v[118:121], v[24:25], off offset:-4096
	global_load_dwordx4 v[102:105], v[24:25], off
	v_fmaak_f32 v5, v5, v126, 0x4b400000
	global_store_dwordx4 v[32:33], v[18:21], off
	global_load_dwordx4 v[94:97], v[24:25], off offset:1024
	global_load_dwordx4 v[82:85], v[24:25], off offset:2048
	s_waitcnt lgkmcnt(12)
	v_mfma_f32_32x32x16_bf16 v[34:49], v[70:73], v[154:157], v[34:49]
	v_add_co_u32_e64 v18, s[4:5], s4, v132
	v_fmaak_f32 v4, v4, v126, 0x4b400000
	s_nop 0
	v_addc_co_u32_e64 v19, s[4:5], 0, v133, s[4:5]
	global_load_dwordx4 v[90:93], v[24:25], off offset:3072
	global_load_dwordx4 v[106:109], v[18:19], off offset:-4096
	global_load_dwordx4 v[122:125], v[22:23], off offset:3072
	global_load_dwordx4 v[98:101], v[2:3], off offset:1024
	global_load_dwordx4 v[86:89], v[2:3], off offset:2048
	global_load_dwordx4 v[70:73], v[2:3], off offset:3072
	v_fmaak_f32 v3, v8, v126, 0x4b400000
	s_waitcnt lgkmcnt(10)
	v_mfma_f32_32x32x16_bf16 v[50:65], v[66:69], v[158:161], v[50:65]
	v_fmaak_f32 v8, v11, v126, 0x4b400000
	v_fmaak_f32 v11, v12, v126, 0x4b400000
	v_fmaak_f32 v2, v9, v126, 0x4b400000
	v_fmaak_f32 v9, v10, v126, 0x4b400000
	v_fmaak_f32 v10, v13, v126, 0x4b400000
	v_fmaak_f32 v7, v7, v126, 0x4b400000
	v_fmaak_f32 v6, v6, v126, 0x4b400000
	s_waitcnt lgkmcnt(8)
	v_mfma_f32_32x32x16_bf16 v[34:49], v[66:69], v[162:165], v[34:49]
	global_load_dwordx4 v[28:31], v[18:19], off
	global_load_dwordx4 v[66:69], v[18:19], off offset:1024
	global_load_dwordx4 v[24:27], v[18:19], off offset:2048
	s_nop 0
	global_load_dwordx4 v[18:21], v[18:19], off offset:3072
	v_perm_b32 v4, v5, v4, s18
	v_perm_b32 v5, v7, v6, s17
	v_perm_b32 v2, v2, v3, s18
	v_or_b32_e32 v5, v5, v2
	v_perm_b32 v2, v8, v9, s17
	v_fmaak_f32 v15, v15, v126, 0x4b400000
	s_waitcnt lgkmcnt(4)
	v_mfma_f32_32x32x16_bf16 v[34:49], v[74:77], v[170:173], v[34:49]
	v_fmaak_f32 v14, v14, v126, 0x4b400000
	v_fmac_f32_e32 v129, v16, v126
	v_fmaak_f32 v16, v17, v126, 0x4b400000
	v_perm_b32 v3, v10, v11, s18
	v_perm_b32 v17, v128, v134, s17
	v_or_b32_e32 v4, v17, v4
	v_mfma_f32_32x32x16_bf16 v[50:65], v[74:77], v[166:169], v[50:65]
	s_waitcnt lgkmcnt(0)
	v_mfma_f32_32x32x16_bf16 v[34:49], v[78:81], v[178:181], v[34:49]
	v_mfma_f32_32x32x16_bf16 v[50:65], v[78:81], v[174:177], v[50:65]
	s_nop 10
	v_max3_f32 v22, |v34|, 0, |v35|
	v_max3_f32 v22, v22, |v36|, |v37|
	v_max3_f32 v22, v22, |v38|, |v39|
	v_max3_f32 v22, v22, |v40|, |v41|
	v_max3_f32 v22, v22, |v42|, |v43|
	v_max3_f32 v22, v22, |v44|, |v45|
	v_max3_f32 v22, v22, |v46|, |v47|
	v_max3_f32 v12, |v50|, 0, |v51|
	v_max3_f32 v12, v12, |v52|, |v53|
	v_max3_f32 v12, v12, |v54|, |v55|
	v_max3_f32 v12, v12, |v56|, |v57|
	v_max3_f32 v12, v12, |v58|, |v59|
	v_max3_f32 v12, v12, |v60|, |v61|
	v_max3_f32 v22, v22, |v48|, |v49|
	v_max3_f32 v12, v12, |v62|, |v63|
	v_mov_b32_e32 v23, v22
	v_max3_f32 v12, v12, |v64|, |v65|
	s_nop 0
	v_permlane32_swap_b32_e32 v22, v23
	v_mov_b32_e32 v13, v12
	v_max_f32_e32 v23, v23, v23
	v_max_f32_e32 v22, v22, v22
	v_permlane32_swap_b32_e32 v12, v13
	v_max_f32_e32 v22, v22, v23
	v_max3_f32 v12, v12, v13, v22
	v_or_b32_e32 v6, v2, v3
	v_perm_b32 v2, v15, v14, s17
	v_perm_b32 v3, v16, v129, s18
	v_or_b32_e32 v7, v2, v3
	global_store_dwordx4 v[32:33], v[4:7], off offset:1024
	v_max_f32_dpp v12, v12, v12 quad_perm:[1,0,3,2] row_mask:0xf bank_mask:0xf
	s_nop 1
	v_max_f32_dpp v12, v12, v12 quad_perm:[2,3,0,1] row_mask:0xf bank_mask:0xf
	s_nop 1
	v_max_f32_dpp v12, v12, v12 row_half_mirror row_mask:0xf bank_mask:0xf
	s_nop 1
	v_max_f32_dpp v12, v12, v12 row_mirror row_mask:0xf bank_mask:0xf
	v_mov_b32_e32 v13, v12
	s_nop 1
	v_permlane16_swap_b32_e32 v13, v12
	v_max_f32_e32 v2, v13, v12
	s_waitcnt lgkmcnt(0)
	s_barrier
	s_and_saveexec_b64 s[4:5], vcc
	v_lshl_add_u32 v1, v1, 2, 0
	ds_write_b32 v1, v2 offset:34816
	s_or_b64 exec, exec, s[4:5]
	s_waitcnt lgkmcnt(0)
	s_barrier
	ds_read_b128 v[2:5], v127 offset:34816
	ds_read_b128 v[6:9], v127 offset:34832
	s_mov_b32 s4, 0x1e3ce508
	v_cmp_eq_u32_e32 vcc, 0, v0
	s_waitcnt lgkmcnt(1)
	v_max_f32_e32 v1, v2, v2
	v_max_f32_e32 v1, 0, v1
	v_max3_f32 v1, v1, v3, v4
	s_waitcnt lgkmcnt(0)
	v_max3_f32 v1, v1, v5, v6
	v_max3_f32 v1, v1, v7, v8
	v_max3_f32 v1, v1, v9, s4
	s_and_saveexec_b64 s[4:5], vcc
	s_cbranch_execz .LBB1_14
	s_load_dwordx2 s[0:1], s[0:1], 0x40
	s_andn2_b32 s2, s2, 63
	s_lshr_b32 s14, s3, 6
	s_or_b32 s14, s14, s2
	s_ashr_i32 s15, s14, 31
	s_lshl_b64 s[14:15], s[14:15], 2
	s_waitcnt lgkmcnt(0)
	s_add_u32 s0, s0, s14
	s_addc_u32 s1, s1, s15
	v_mov_b32_e32 v2, 0
	v_mul_f32_e32 v3, 0x3c010204, v1
	global_store_dword v2, v3, s[0:1]
